# v69 variant: round 0 = gelu(0), gelu-stat(2), rope-q, rope-q; round 1 = gelu(1), gelu-stat(3), rope-k, rope-k
# baseline (speedup 1.0000x reference)
;     __device__ bool next(int i, Unit& u) const { if (!base.next(i >> 1, u)) return false; if (i & 1) { u.pm += MTOK / BM; u.pn += DM / BM; } return true; }
;   __device__ __forceinline__ bool next(int i,AttnUnit&u)const{ if(i>=2||vcu>=256)return false; const int s=vcu&3; u.bh=vcu>>2; u.qb=(i==0)?7-s:s; return true; }
;     __host__ __device__ bool next(int i, Unit& u) const {
;         const int L = i * G + c; if (L >= nwg) return false;
;         int wgid = L; { const int q = nwg / NXCD, r = nwg % NXCD, xcd = wgid % NXCD, off = wgid / NXCD; wgid = (xcd < r ? xcd * (q + 1) : r * (q + 1) + (xcd - r) * q) + off; }
;         const int nig = WGM * nN, gid = wgid / nig, fm = gid * WGM, gsz = (nM - fm) < WGM ? (nM - fm) : WGM;
;         u.pm = fm + ((wgid % nig) % gsz); u.pn = (wgid % nig) / gsz; u.half = 0; return true;
.LBB0_382:
	s_ashr_i32 s4, s21, 31
	s_lshr_b32 s4, s4, 29
	s_add_i32 s4, s21, s4
	s_ashr_i32 s5, s4, 3
	s_and_b32 s4, s4, -8
	s_sub_i32 s4, s21, s4
	s_cmp_lt_i32 s4, 0
	s_movk_i32 s6, 0x91
	s_cselect_b32 s6, s6, 0x90
	s_mul_i32 s4, s4, s6
	s_add_i32 s4, s4, s5
	s_mul_hi_i32 s5, s4, 0x38e38e39
	s_lshr_b32 s6, s5, 31
	s_ashr_i32 s5, s5, 5
	s_add_i32 s5, s5, s6
	s_lshl_b32 s6, s5, 3
	s_mulk_i32 s5, 0x90
	s_sub_i32 s4, s4, s5
	s_bfe_u32 s5, s4, 0x3001c
	s_add_i32 s5, s4, s5
	s_sext_i32_i16 s7, s5
	s_and_b32 s5, s5, 0xfff8
	s_sub_i32 s4, s4, s5
	s_sext_i32_i16 s4, s4
	s_add_i32 s18, s6, s4
	s_ashr_i32 s70, s7, 3
	s_mul_i32 s4, s70, 5
	s_cmp_lt_u32 s70, 12
	s_cbranch_scc0 .Lpn_hi0
	s_mov_b32 s6, 0x86129040
	s_mov_b32 s7, 0x5a92839
	s_branch .Lpn_go0

;     __device__ bool next(int i, Unit& u) const { if (!base.next(i >> 1, u)) return false; if (i & 1) { u.pm += MTOK / BM; u.pn += DM / BM; } return true; }
;   __device__ __forceinline__ bool next(int i,AttnUnit&u)const{ if(i>=2||vcu>=256)return false; const int s=vcu&3; u.bh=vcu>>2; u.qb=(i==0)?7-s:s; return true; }
;     __host__ __device__ bool next(int i, Unit& u) const {
;         const int L = i * G + c; if (L >= nwg) return false;
;         int wgid = L; { const int q = nwg / NXCD, r = nwg % NXCD, xcd = wgid % NXCD, off = wgid / NXCD; wgid = (xcd < r ? xcd * (q + 1) : r * (q + 1) + (xcd - r) * q) + off; }
;         const int nig = WGM * nN, gid = wgid / nig, fm = gid * WGM, gsz = (nM - fm) < WGM ? (nM - fm) : WGM;
;         u.pm = fm + ((wgid % nig) % gsz); u.pn = (wgid % nig) / gsz; u.half = 0; return true;
; template <class Epi, class Sched, bool ALIGN_EPI = false, bool SP2 = false>
; __device__ __forceinline__ void gemm_phase(PG8_LAS unsigned char* lds, const Gemm g, const Sched& S, const Epi& E) {
;     ...
;         const bool has_next = S.next(ui + 1, nxt);
;         const char* nA = has_next ? (const char*)g.A + (size_t)nxt.pm * tstep + (nxt.half == 2 ? hstep : (size_t)0) : cA; const char* nB = has_next ? (const char*)g.Bt + (size_t)nxt.pn * tstep : cB;
.LBB0_392:
	s_add_i32 s72, s72, 1
	s_mul_i32 s10, s72, s33
	s_add_i32 s10, s10, s21
	s_cmpk_lt_i32 s10, 0x480
	s_cselect_b64 s[64:65], -1, 0
	s_cmpk_gt_i32 s10, 0x47f
	s_cbranch_scc1 .LBB0_394
	s_ashr_i32 s11, s10, 31
	s_lshr_b32 s11, s11, 29
	s_add_i32 s11, s10, s11
	s_ashr_i32 s12, s11, 3
	s_and_b32 s11, s11, -8
	s_sub_i32 s10, s10, s11
	s_cmp_lt_i32 s10, 0
	s_movk_i32 s11, 0x91
	s_cselect_b32 s11, s11, 0x90
	s_mul_i32 s10, s10, s11
	s_add_i32 s10, s10, s12
	s_mul_hi_i32 s11, s10, 0x38e38e39
	s_lshr_b32 s12, s11, 31
	s_ashr_i32 s11, s11, 5
	s_add_i32 s11, s11, s12
	s_lshl_b32 s12, s11, 3
	s_mulk_i32 s11, 0x90
	s_sub_i32 s10, s10, s11
	s_bfe_u32 s11, s10, 0x3001c
	s_add_i32 s11, s10, s11
	s_sext_i32_i16 s13, s11
	s_and_b32 s11, s11, 0xfff8
	s_sub_i32 s10, s10, s11
	s_sext_i32_i16 s10, s10
	s_add_i32 s60, s12, s10
	s_ashr_i32 s62, s13, 3
	s_mul_i32 s10, s62, 5
	s_cmp_lt_u32 s62, 12
	s_cbranch_scc0 .Lpn_hi1
	s_mov_b32 s12, 0x86129040
	s_mov_b32 s13, 0x5a92839
	s_branch .Lpn_go1
